# pools: prologue 896 items, 768 layer-1 items in dense-up idle round (quota 6), attention pools 4112/4112, post-attention quota 1; early claim; adaLN 2x unroll
# baseline (speedup 1.0000x reference)
.LBB0_28:
	s_or_b64 exec, exec, s[2:3]
	s_add_u32 s4, s94, 0x9c00000
	s_addc_u32 s5, s95, 0
	s_add_u32 s6, s94, 0x7000000
	s_addc_u32 s7, s95, 0
	s_add_u32 s33, s94, 0x6000000
	s_addc_u32 s52, s95, 0
	s_add_u32 s53, s94, 0x5800000
	s_addc_u32 s54, s95, 0
	s_add_u32 s55, s94, 0x5000000
	s_addc_u32 s56, s95, 0
	s_add_u32 s57, s94, 0x800000
	s_addc_u32 s58, s95, 0
	s_add_i32 s2, 0, 0x20180
	v_mov_b32_e32 v1, s2
	s_waitcnt lgkmcnt(0)
	s_waitcnt lgkmcnt(0)
	s_barrier
	ds_read_b32 v3, v1
	s_movk_i32 s3, 0x37f
	v_lshrrev_b32_e32 v1, 1, v0
	s_movk_i32 s2, 0x380
	v_and_b32_e32 v1, 0xf0, v1
	s_waitcnt lgkmcnt(0)
	v_cmp_lt_i32_e32 vcc, s3, v3
	v_and_b32_e32 v75, 0x7c, v2
	v_readfirstlane_b32 s13, v3
	v_cmp_gt_i32_e64 s[2:3], s2, v3
	s_cbranch_vccnz .LBB0_34
	s_cmpk_gt_i32 s13, 0x67f
	s_cbranch_scc0 .LBB0_35
	s_cmpk_gt_u32 s13, 0x7df
	s_cbranch_scc0 .LBB0_36
	s_cmpk_gt_u32 s13, 0x93f
	s_cbranch_scc0 .LBB0_44
	s_add_i32 s12, s13, 0xfffff6c0
	s_mov_b64 s[10:11], s[82:83]
	s_mov_b32 s27, 1
	s_cbranch_execz .LBB0_45
	s_movk_i32 s14, 0x800
	s_mov_b32 s26, 0
	s_movk_i32 s25, 0x1600
	s_mov_b64 s[68:69], s[4:5]
	s_cbranch_execz .LBB0_37
	s_branch .LBB0_38

.LBB0_57:
	v_lshlrev_b32_e32 v68, 4, v0
	v_lshrrev_b32_e32 v76, 5, v0
	v_and_b32_e32 v66, 31, v0
	v_and_b32_e32 v67, 0x1e0, v0
	v_lshrrev_b32_e32 v79, 4, v0
	v_and_b32_e32 v70, 0xf0, v68
	v_add_u32_e32 v67, 0, v67
	v_mul_u32_u24_e32 v77, 0x840, v66
	v_add_u32_e32 v68, 0, v70
	v_mov_b32_e32 v73, 0
	v_mul_u32_u24_e32 v69, 0x210, v79
	v_lshl_add_u32 v72, v66, 4, 0
	v_lshlrev_b32_e32 v74, 3, v66
	v_mul_u32_u24_e32 v66, 0x210, v76
	s_mov_b32 s11, 0
	v_lshl_add_u32 v78, v76, 4, 0
	v_mov_b32_e32 v71, v73
	v_or_b32_e32 v80, 64, v79
	v_or_b32_e32 v81, 32, v76
	v_or_b32_e32 v82, 64, v76
	v_or_b32_e32 v83, 0x60, v76
	s_mov_b32 s12, 0x7ffffffe
	s_mov_b32 s13, 0xc2fe0000
	s_mov_b32 s14, 0x4b400000
	v_add_u32_e32 v84, v67, v77
	s_add_i32 s15, 0, 0x20184
	s_movk_i32 s20, 0x37f
	v_mov_b32_e32 v85, 0x42fe0000
	v_add_u32_e32 v86, v68, v69
	v_add_u32_e32 v87, v72, v66
	s_branch .LBB0_60

.LBB0_75:
	v_mov_b32_e32 v66, 0x380

.LBB0_1511:
	s_or_b64 exec, exec, s[12:13]
	s_waitcnt vmcnt(0)
	v_readfirstlane_b32 s10, v3
	s_nop 1
	v_add_u32_e32 v2, s10, v2
	s_add_i32 s10, 0, 0x20180
	v_add_u32_e32 v2, 0x380, v2
	v_mov_b32_e32 v3, s10
	ds_write_b32 v3, v2

.LBB0_1568:
	s_or_b64 exec, exec, s[28:29]
	s_waitcnt vmcnt(0)
	v_readfirstlane_b32 s6, v67
	s_nop 1
	v_add_u32_e32 v66, s6, v66
	v_add_u32_e32 v66, 0x380, v66
